# speedup vs baseline: 1.0022x; 1.0022x over previous
.LBB7_14:
	s_lshl_b32 s11, s23, 14
	v_add_u32_e32 v36, s11, v14
	v_or_b32_e32 v37, s11, v18
	v_add_u32_e32 v38, v36, v17
	v_add_u32_e32 v39, v37, v17
	v_add_u32_e32 v56, v36, v19
	v_add_u32_e32 v57, v37, v19
	ds_read_b128 v[20:23], v38
	ds_read_b128 v[24:27], v39 offset:8192
	ds_read_b128 v[28:31], v38 offset:2048
	ds_read_b128 v[32:35], v39 offset:10240
	ds_read_b128 v[40:43], v56
	ds_read_b128 v[44:47], v57 offset:8192
	ds_read_b128 v[48:51], v56 offset:2048
	ds_read_b128 v[52:55], v57 offset:10240
	s_add_i32 s11, s23, 1
	s_cmp_lg_u32 s23, 3
	s_cselect_b32 s23, s11, 0
	s_add_i32 s11, s22, 1
	s_cmp_lg_u32 s22, 3
	s_cselect_b32 s22, s11, 0
	s_add_i32 s24, s24, 1
	s_add_i32 s21, s21, -1
	s_cmp_eq_u32 s21, -1
	s_waitcnt lgkmcnt(4)
	v_mfma_f32_16x16x32_f16 a[12:15], v[28:31], v[32:35], a[12:15]
	v_mfma_f32_16x16x32_f16 a[0:3], v[20:23], v[24:27], a[0:3]
	v_mfma_f32_16x16x32_f16 a[4:7], v[20:23], v[32:35], a[4:7]
	v_mfma_f32_16x16x32_f16 a[8:11], v[28:31], v[24:27], a[8:11]
	s_waitcnt lgkmcnt(0)
	v_mfma_f32_16x16x32_f16 a[0:3], v[40:43], v[44:47], a[0:3]
	v_mfma_f32_16x16x32_f16 a[4:7], v[40:43], v[52:55], a[4:7]
	v_mfma_f32_16x16x32_f16 a[8:11], v[48:51], v[44:47], a[8:11]
	v_mfma_f32_16x16x32_f16 a[12:15], v[48:51], v[52:55], a[12:15]
	s_cbranch_scc1 .LBB7_26

	.amdhsa_kernel _Z6gemm_gILi64ELi64ELi32ELi32ELi1ELi0ELi64ELi4EEv5GemmP
		.amdhsa_group_segment_fixed_size 65536
		.amdhsa_private_segment_fixed_size 0
		.amdhsa_kernarg_size 112
		.amdhsa_user_sgpr_count 2
		.amdhsa_user_sgpr_dispatch_ptr 0
		.amdhsa_user_sgpr_queue_ptr 0
		.amdhsa_user_sgpr_kernarg_segment_ptr 1
		.amdhsa_user_sgpr_dispatch_id 0
		.amdhsa_user_sgpr_kernarg_preload_length 0
		.amdhsa_user_sgpr_kernarg_preload_offset 0
		.amdhsa_user_sgpr_private_segment_size 0
		.amdhsa_uses_dynamic_stack 0
		.amdhsa_enable_private_segment 0
		.amdhsa_system_sgpr_workgroup_id_x 1
		.amdhsa_system_sgpr_workgroup_id_y 1
		.amdhsa_system_sgpr_workgroup_id_z 0
		.amdhsa_system_sgpr_workgroup_info 0
		.amdhsa_system_vgpr_workitem_id 0
		.amdhsa_next_free_vgpr 169
		.amdhsa_next_free_sgpr 96
		.amdhsa_accum_offset 60
		.amdhsa_reserve_vcc 1
		.amdhsa_float_round_mode_32 0
		.amdhsa_float_round_mode_16_64 0
		.amdhsa_float_denorm_mode_32 3
		.amdhsa_float_denorm_mode_16_64 3
		.amdhsa_dx10_clamp 1
		.amdhsa_ieee_mode 1
		.amdhsa_fp16_overflow 0
		.amdhsa_tg_split 0
		.amdhsa_exception_fp_ieee_invalid_op 0
		.amdhsa_exception_fp_denorm_src 0
		.amdhsa_exception_fp_ieee_div_zero 0
		.amdhsa_exception_fp_ieee_overflow 0
		.amdhsa_exception_fp_ieee_underflow 0
		.amdhsa_exception_fp_ieee_inexact 0
		.amdhsa_exception_int_div_zero 0
	.end_amdhsa_kernel

.LBB9_6:
	s_lshl_b32 s0, s22, 14
	v_add_u32_e32 v28, s0, v1
	v_or_b32_e32 v29, s0, v5
	v_add_u32_e32 v56, v28, v0
	v_add_u32_e32 v57, v29, v0
	v_add_u32_e32 v58, v28, v7
	v_add_u32_e32 v59, v29, v7
	ds_read_b128 v[12:15], v56
	ds_read_b128 v[16:19], v57 offset:8192
	ds_read_b128 v[20:23], v56 offset:2048
	ds_read_b128 v[24:27], v57 offset:10240
	ds_read_b128 v[40:43], v58
	ds_read_b128 v[44:47], v59 offset:8192
	ds_read_b128 v[48:51], v58 offset:2048
	ds_read_b128 v[52:55], v59 offset:10240
	s_add_i32 s0, s22, 1
	s_cmp_lg_u32 s22, 2
	s_cselect_b32 s22, s0, 0
	s_add_i32 s0, s21, 1
	s_cmp_lg_u32 s21, 2
	s_cselect_b32 s21, s0, 0
	s_add_i32 s15, s15, 1
	s_cmp_eq_u32 s12, s15
	s_waitcnt lgkmcnt(4)
	v_mfma_f32_16x16x32_f16 a[0:3], v[20:23], v[24:27], a[0:3]
	v_mfma_f32_16x16x32_f16 a[12:15], v[12:15], v[16:19], a[12:15]
	v_mfma_f32_16x16x32_f16 a[8:11], v[12:15], v[24:27], a[8:11]
	v_mfma_f32_16x16x32_f16 a[4:7], v[20:23], v[16:19], a[4:7]
	s_waitcnt lgkmcnt(0)
	v_mfma_f32_16x16x32_f16 a[12:15], v[40:43], v[44:47], a[12:15]
	v_mfma_f32_16x16x32_f16 a[8:11], v[40:43], v[52:55], a[8:11]
	v_mfma_f32_16x16x32_f16 a[4:7], v[48:51], v[44:47], a[4:7]
	v_mfma_f32_16x16x32_f16 a[0:3], v[48:51], v[52:55], a[0:3]
	s_cbranch_scc1 .LBB9_13

	.amdhsa_kernel _Z6gemm_gILi64ELi64ELi32ELi32ELi0ELi3ELi64ELi3EEv5GemmP
		.amdhsa_group_segment_fixed_size 49152
		.amdhsa_private_segment_fixed_size 0
		.amdhsa_kernarg_size 112
		.amdhsa_user_sgpr_count 2
		.amdhsa_user_sgpr_dispatch_ptr 0
		.amdhsa_user_sgpr_queue_ptr 0
		.amdhsa_user_sgpr_kernarg_segment_ptr 1
		.amdhsa_user_sgpr_dispatch_id 0
		.amdhsa_user_sgpr_kernarg_preload_length 0
		.amdhsa_user_sgpr_kernarg_preload_offset 0
		.amdhsa_user_sgpr_private_segment_size 0
		.amdhsa_uses_dynamic_stack 0
		.amdhsa_enable_private_segment 0
		.amdhsa_system_sgpr_workgroup_id_x 1
		.amdhsa_system_sgpr_workgroup_id_y 1
		.amdhsa_system_sgpr_workgroup_id_z 0
		.amdhsa_system_sgpr_workgroup_info 0
		.amdhsa_system_vgpr_workitem_id 0
		.amdhsa_next_free_vgpr 129
		.amdhsa_next_free_sgpr 96
		.amdhsa_accum_offset 60
		.amdhsa_reserve_vcc 1
		.amdhsa_float_round_mode_32 0
		.amdhsa_float_round_mode_16_64 0
		.amdhsa_float_denorm_mode_32 3
		.amdhsa_float_denorm_mode_16_64 3
		.amdhsa_dx10_clamp 1
		.amdhsa_ieee_mode 1
		.amdhsa_fp16_overflow 0
		.amdhsa_tg_split 0
		.amdhsa_exception_fp_ieee_invalid_op 0
		.amdhsa_exception_fp_denorm_src 0
		.amdhsa_exception_fp_ieee_div_zero 0
		.amdhsa_exception_fp_ieee_overflow 0
		.amdhsa_exception_fp_ieee_underflow 0
		.amdhsa_exception_fp_ieee_inexact 0
		.amdhsa_exception_int_div_zero 0
	.end_amdhsa_kernel

.LBB10_6:
	s_lshl_b32 s9, s18, 14
	v_add_u32_e32 v17, s9, v13
	v_or_b32_e32 v34, s9, v15
	v_add_u32_e32 v52, v17, v14
	v_add_u32_e32 v53, v34, v14
	v_add_u32_e32 v54, v17, v16
	v_add_u32_e32 v55, v34, v16
	ds_read_b128 v[18:21], v52
	ds_read_b128 v[22:25], v53 offset:8192
	ds_read_b128 v[26:29], v52 offset:2048
	ds_read_b128 v[30:33], v53 offset:10240
	ds_read_b128 v[36:39], v54
	ds_read_b128 v[40:43], v55 offset:8192
	ds_read_b128 v[44:47], v54 offset:2048
	ds_read_b128 v[48:51], v55 offset:10240
	s_add_i32 s9, s18, 1
	s_cmp_lg_u32 s18, 2
	s_cselect_b32 s18, s9, 0
	s_add_i32 s9, s14, 1
	s_cmp_lg_u32 s14, 2
	s_cselect_b32 s14, s9, 0
	s_add_i32 s19, s19, 1
	s_cmp_eq_u32 s15, s19
	s_waitcnt lgkmcnt(4)
	v_mfma_f32_16x16x32_f16 a[12:15], v[26:29], v[30:33], a[12:15]
	v_mfma_f32_16x16x32_f16 a[0:3], v[18:21], v[22:25], a[0:3]
	v_mfma_f32_16x16x32_f16 a[4:7], v[18:21], v[30:33], a[4:7]
	v_mfma_f32_16x16x32_f16 a[8:11], v[26:29], v[22:25], a[8:11]
	s_waitcnt lgkmcnt(0)
	v_mfma_f32_16x16x32_f16 a[0:3], v[36:39], v[40:43], a[0:3]
	v_mfma_f32_16x16x32_f16 a[4:7], v[36:39], v[48:51], a[4:7]
	v_mfma_f32_16x16x32_f16 a[8:11], v[44:47], v[40:43], a[8:11]
	v_mfma_f32_16x16x32_f16 a[12:15], v[44:47], v[48:51], a[12:15]
	s_cbranch_scc1 .LBB10_13

	.amdhsa_kernel _Z6gemm_gILi64ELi64ELi32ELi32ELi0ELi4ELi64ELi3EEv5GemmP
		.amdhsa_group_segment_fixed_size 49152
		.amdhsa_private_segment_fixed_size 0
		.amdhsa_kernarg_size 112
		.amdhsa_user_sgpr_count 2
		.amdhsa_user_sgpr_dispatch_ptr 0
		.amdhsa_user_sgpr_queue_ptr 0
		.amdhsa_user_sgpr_kernarg_segment_ptr 1
		.amdhsa_user_sgpr_dispatch_id 0
		.amdhsa_user_sgpr_kernarg_preload_length 0
		.amdhsa_user_sgpr_kernarg_preload_offset 0
		.amdhsa_user_sgpr_private_segment_size 0
		.amdhsa_uses_dynamic_stack 0
		.amdhsa_enable_private_segment 0
		.amdhsa_system_sgpr_workgroup_id_x 1
		.amdhsa_system_sgpr_workgroup_id_y 1
		.amdhsa_system_sgpr_workgroup_id_z 0
		.amdhsa_system_sgpr_workgroup_info 0
		.amdhsa_system_vgpr_workitem_id 0
		.amdhsa_next_free_vgpr 129
		.amdhsa_next_free_sgpr 96
		.amdhsa_accum_offset 56
		.amdhsa_reserve_vcc 1
		.amdhsa_float_round_mode_32 0
		.amdhsa_float_round_mode_16_64 0
		.amdhsa_float_denorm_mode_32 3
		.amdhsa_float_denorm_mode_16_64 3
		.amdhsa_dx10_clamp 1
		.amdhsa_ieee_mode 1
		.amdhsa_fp16_overflow 0
		.amdhsa_tg_split 0
		.amdhsa_exception_fp_ieee_invalid_op 0
		.amdhsa_exception_fp_denorm_src 0
		.amdhsa_exception_fp_ieee_div_zero 0
		.amdhsa_exception_fp_ieee_overflow 0
		.amdhsa_exception_fp_ieee_underflow 0
		.amdhsa_exception_fp_ieee_inexact 0
		.amdhsa_exception_int_div_zero 0
	.end_amdhsa_kernel
